# v71 + WGs 0..119 hand their second Fourier stage-2 unit to WGs 136..255 (layer-0 mixers load balance)
# baseline (speedup 1.0000x reference)
; DI void fft3_unit(unsigned char* lds, const unsigned char* ws, int unit) {
;     int tid = threadIdx.x; asm volatile("" : "+v"(tid));
;     const int lane = tid & 63, r = lane & 31, h = lane >> 5, w = tid >> 6, b = unit >> 6, k1 = unit & 63;
;     const bf16_t* Y2 = (const bf16_t*)(ws + WS_Y2) + (size_t)unit * 256 * 128;
;     unsigned char* Bt = lds + FF3_B;
;     { u32x4 v[8];
; #pragma unroll
;       for (int j = 0; j < 8; ++j) { const int idx = tid + 512 * j; v[j] = *(const u32x4*)(Y2 + (size_t)idx * 8); }
; #pragma unroll
;       for (int j = 0; j < 8; ++j) { const int idx = tid + 512 * j; *(u32x4*)(Bt + (idx >> 4) * FF_PITCH + 16 * (idx & 15)) = v[j]; } }
;     __syncthreads();
; template <int li>
; DI void layer_phases(unsigned char* smem, LAS unsigned char* ldsL, const int lo, const int hi) {
;     ...
;               fft_load_a(smem + FF3_A, WSP(const bf16_t, WS_M3), 64);
;               for (int L = blockIdx.x; L < 512; L += gridDim.x) fft3_unit(smem, ws, L); }
.LBB0_683:
	s_or_b64 exec, exec, s[8:9]
	s_and_b64 vcc, exec, s[4:5]
	s_waitcnt lgkmcnt(0)
	s_barrier
	s_cbranch_vccnz .LBB0_686
	s_add_u32 s8, s6, 0x19094000
	s_addc_u32 s9, s7, 0
	s_lshl_b32 s10, s2, 6
	s_lshl_b32 s11, s64, 6
	s_movk_i32 s12, 0x110
	s_movk_i32 s13, 0xffe0
	v_mov_b32_e32 v35, 0
	s_mov_b32 s14, 0xc3e00000
	v_mov_b32_e32 v36, 0x43e00000
	s_mov_b32 s15, 0x2add4000
	s_mov_b32 s16, 0x2ade4000
	s_mov_b32 s17, 0x2adf4000
	s_mov_b32 s18, 0x2ae04000
	s_mov_b32 s19, 0x2ae54000
	s_mov_b32 s20, 0x2ae64000
	s_mov_b32 s21, 0x2ae74000
	s_mov_b32 s22, 0x2ae84000
	s_mov_b32 s23, 0x2aed4000
	s_mov_b32 s24, 0x2aee4000
	s_mov_b32 s25, 0x2aef4000
	s_mov_b32 s28, 0x2af04000
	s_mov_b32 s29, 0x2af54000
	s_mov_b32 s36, 0x2af64000
	s_mov_b32 s37, 0x2af74000
	s_mov_b32 s38, 0x2af84000
	s_mov_b32 s39, 0x2afd4000
	s_mov_b32 s40, 0x2afe4000
	s_mov_b32 s41, 0x2aff4000
	s_mov_b32 s42, 0x2b004000
	s_mov_b32 s43, 0x2b054000
	s_mov_b32 s46, 0x2b064000
	s_mov_b32 s47, 0x2b074000
	s_mov_b32 s48, 0x2b084000
	s_mov_b32 s49, 0x2b0d4000
	s_mov_b32 s52, 0x2b0e4000
	s_mov_b32 s53, 0x2b0f4000
	s_mov_b32 s54, 0x2b104000
	s_mov_b32 s55, 0x2b154000
	s_mov_b32 s56, 0x2b164000
	s_mov_b32 s57, 0x2b174000
	s_mov_b32 s4, s2
	s_add_i32 s72, s2, 0x100
	s_add_i32 s74, s2, 0x78
	s_movk_i32 s73, 0x200
	s_cmp_lt_u32 s2, 0x78
	s_cselect_b32 s72, 0x200, s72
	s_cmp_gt_u32 s2, 0x87
	s_cselect_b32 s73, s74, s73
.LBB0_685:
	s_ashr_i32 s5, s4, 31
	v_mov_b32_e32 v2, v0
	s_lshl_b64 s[58:59], s[4:5], 16
	s_add_u32 s58, s8, s58
	v_add_u32_e32 v4, 0x200, v2
	v_add_u32_e32 v6, 0x400, v2
	v_add_u32_e32 v8, 0x600, v2
	v_add_u32_e32 v10, 0x800, v2
	v_add_u32_e32 v12, 0xa00, v2
	v_add_u32_e32 v14, 0xc00, v2
	v_add_u32_e32 v16, 0xe00, v2
	v_bfe_u32 v66, v2, 5, 1
	v_lshlrev_b32_e32 v18, 4, v2
	v_ashrrev_i32_e32 v19, 1, v2
	v_ashrrev_i32_e32 v3, 31, v2
	s_addc_u32 s59, s9, s59
	v_ashrrev_i32_e32 v5, 31, v4
	v_ashrrev_i32_e32 v7, 31, v6
	v_ashrrev_i32_e32 v9, 31, v8
	v_ashrrev_i32_e32 v11, 31, v10
	v_ashrrev_i32_e32 v13, 31, v12
	v_ashrrev_i32_e32 v15, 31, v14
	v_ashrrev_i32_e32 v17, 31, v16
	v_and_b32_e32 v49, 0xf0, v18
	v_and_b32_e32 v48, 0xffffffe0, v19
	v_bfi_b32 v19, s13, v19, v2
	v_lshl_add_u32 v18, v66, 4, 0
	v_lshrrev_b32_e32 v51, 4, v2
	v_and_b32_e32 v34, 31, v2
	v_lshl_add_u64 v[2:3], v[2:3], 4, s[58:59]
	v_lshl_add_u64 v[20:21], v[4:5], 4, s[58:59]
	v_lshl_add_u64 v[22:23], v[6:7], 4, s[58:59]
	v_lshl_add_u64 v[24:25], v[8:9], 4, s[58:59]
	v_lshl_add_u64 v[26:27], v[10:11], 4, s[58:59]
	v_lshl_add_u64 v[28:29], v[12:13], 4, s[58:59]
	v_lshl_add_u64 v[30:31], v[14:15], 4, s[58:59]
	v_lshl_add_u64 v[32:33], v[16:17], 4, s[58:59]
	v_mad_u64_u32 v[68:69], s[58:59], v19, s12, v[18:19]
	v_lshrrev_b32_e32 v54, 4, v4
	v_lshrrev_b32_e32 v56, 4, v6
	v_lshrrev_b32_e32 v58, 4, v8
	v_lshrrev_b32_e32 v60, 4, v10
	v_lshrrev_b32_e32 v62, 4, v12
	v_lshrrev_b32_e32 v64, 4, v14
	v_lshrrev_b32_e32 v67, 4, v16
	v_mad_u32_u24 v69, v34, s12, v18
	global_load_dwordx4 v[2:5], v[2:3], off
	s_nop 0
	global_load_dwordx4 v[6:9], v[20:21], off
	global_load_dwordx4 v[10:13], v[22:23], off
	global_load_dwordx4 v[14:17], v[24:25], off
	s_nop 0
	global_load_dwordx4 v[18:21], v[26:27], off
	global_load_dwordx4 v[22:25], v[28:29], off
	s_nop 0
	global_load_dwordx4 v[26:29], v[30:31], off
	s_nop 0
	global_load_dwordx4 v[30:33], v[32:33], off
	s_and_b32 s5, s4, 63
	s_and_b32 s60, s10, 0xfffff000
	s_or_b32 s58, s60, s5
	s_ashr_i32 s59, s58, 31
	s_lshl_b64 s[58:59], s[58:59], 10
	s_add_u32 s58, s6, s58
	v_add_u32_e32 v50, 0, v49
	v_ashrrev_i32_e32 v49, 31, v48
	s_addc_u32 s59, s7, s59
	v_lshl_add_u64 v[48:49], s[58:59], 0, v[48:49]
	v_mad_u64_u32 v[52:53], s[60:61], v51, s12, v[50:51]
	v_mad_u64_u32 v[54:55], s[60:61], v54, s12, v[50:51]
	v_mad_u64_u32 v[56:57], s[60:61], v56, s12, v[50:51]
	v_mad_u64_u32 v[58:59], s[60:61], v58, s12, v[50:51]
	v_mad_u64_u32 v[60:61], s[60:61], v60, s12, v[50:51]
	v_mad_u64_u32 v[62:63], s[60:61], v62, s12, v[50:51]
	v_mad_u64_u32 v[64:65], s[60:61], v64, s12, v[50:51]
	v_mad_u64_u32 v[50:51], s[60:61], v67, s12, v[50:51]
	v_lshl_add_u64 v[48:49], v[48:49], 0, v[34:35]
	v_lshlrev_b32_e32 v34, 18, v66
	v_lshl_add_u64 v[70:71], v[48:49], 0, v[34:35]
	v_add_co_u32_e32 v72, vcc, s15, v70
	v_mov_b32_e32 v37, v35
	s_nop 0
	v_addc_co_u32_e32 v73, vcc, 0, v71, vcc
	v_add_co_u32_e32 v74, vcc, s16, v70
	s_waitcnt vmcnt(7)
	ds_write_b128 v52, v[2:5] offset:17408
	s_waitcnt vmcnt(6)
	ds_write_b128 v54, v[6:9] offset:17408
	s_waitcnt vmcnt(5)
	ds_write_b128 v56, v[10:13] offset:17408
	s_waitcnt vmcnt(4)
	ds_write_b128 v58, v[14:17] offset:17408
	s_waitcnt vmcnt(3)
	ds_write_b128 v60, v[18:21] offset:17408
	s_waitcnt vmcnt(2)
	ds_write_b128 v62, v[22:25] offset:17408
	s_waitcnt vmcnt(1)
	ds_write_b128 v64, v[26:29] offset:17408
	s_waitcnt vmcnt(0)
	ds_write_b128 v50, v[30:33] offset:17408
	s_waitcnt lgkmcnt(0)
	s_barrier
; DI f32x16 mfma32(bf16x8 a, bf16x8 b, f32x16 c) { return __builtin_amdgcn_mfma_f32_32x32x16_bf16(a, b, c, 0, 0, 0); }
; DI void fft3_unit(unsigned char* lds, const unsigned char* ws, int unit) {
;     ...
;     f32x16 acc[2];
;     acc[0] = (f32x16){}; acc[1] = (f32x16){};
; #pragma unroll
;     for (int ks = 0; ks < 8; ++ks) { const bf16x8 bf = *(const bf16x8*)(Bt + (32 * w + r) * FF_PITCH + 32 * ks + 16 * h);
; #pragma unroll
;         for (int rb = 0; rb < 2; ++rb) acc[rb] = mfma32(*(const bf16x8*)(lds + FF3_A + (32 * rb + r) * FF_PITCH + 32 * ks + 16 * h), bf, acc[rb]); }
;     unsigned char* CAT = const_cast<unsigned char*>(ws) + WS_CAT + (size_t)(b * SEQ + k1) * 1024 + 512 + 32 * w + r;
	ds_read_b128 v[2:5], v69
	ds_read_b128 v[6:9], v68 offset:17408
	ds_read_b128 v[48:51], v68 offset:17440
	ds_read_b128 v[52:55], v69 offset:32
	s_waitcnt lgkmcnt(2)
	v_mfma_f32_32x32x16_bf16 v[18:33], v[2:5], v[6:9], 0
	ds_read_b128 v[2:5], v69 offset:8704
	ds_read_b128 v[56:59], v69 offset:8736
	v_addc_co_u32_e32 v75, vcc, 0, v71, vcc
	v_add_co_u32_e32 v76, vcc, s17, v70
	v_mov_b32_e32 v38, v35
	s_nop 0
	v_addc_co_u32_e32 v77, vcc, 0, v71, vcc
	s_waitcnt lgkmcnt(1)
	v_mfma_f32_32x32x16_bf16 v[2:17], v[2:5], v[6:9], 0
	v_add_co_u32_e32 v78, vcc, s18, v70
	v_mov_b32_e32 v39, v35
	s_nop 0
	v_addc_co_u32_e32 v79, vcc, 0, v71, vcc
	v_add_co_u32_e32 v80, vcc, s19, v70
	v_mfma_f32_32x32x16_bf16 v[18:33], v[52:55], v[48:51], v[18:33]
	s_nop 0
	v_addc_co_u32_e32 v81, vcc, 0, v71, vcc
	v_add_co_u32_e32 v82, vcc, s20, v70
	v_mov_b32_e32 v40, v35
	s_nop 0
	v_addc_co_u32_e32 v83, vcc, 0, v71, vcc
	s_waitcnt lgkmcnt(0)
	v_mfma_f32_32x32x16_bf16 v[2:17], v[56:59], v[48:51], v[2:17]
	ds_read_b128 v[48:51], v69 offset:64
	ds_read_b128 v[52:55], v68 offset:17472
	ds_read_b128 v[56:59], v68 offset:17504
	ds_read_b128 v[60:63], v69 offset:96
	v_add_co_u32_e32 v84, vcc, s21, v70
	s_mov_b32 s4, s72
	s_mov_b32 s72, s73
	s_movk_i32 s73, 0x200
	s_nop 0
	v_addc_co_u32_e32 v85, vcc, 0, v71, vcc
	v_add_co_u32_e32 v86, vcc, s22, v70
	s_waitcnt lgkmcnt(2)
	v_mfma_f32_32x32x16_bf16 v[18:33], v[48:51], v[52:55], v[18:33]
	ds_read_b128 v[48:51], v69 offset:8768
	ds_read_b128 v[64:67], v69 offset:8800
	v_addc_co_u32_e32 v87, vcc, 0, v71, vcc
	v_add_co_u32_e32 v88, vcc, s23, v70
	s_lshl_b32 s10, s4, 6
	s_nop 0
	v_addc_co_u32_e32 v89, vcc, 0, v71, vcc
	s_waitcnt lgkmcnt(1)
	v_mfma_f32_32x32x16_bf16 v[2:17], v[48:51], v[52:55], v[2:17]
	v_add_co_u32_e32 v90, vcc, s24, v70
	v_mov_b32_e32 v41, v35
	s_nop 0
	v_addc_co_u32_e32 v91, vcc, 0, v71, vcc
	v_add_co_u32_e32 v92, vcc, s25, v70
	v_mfma_f32_32x32x16_bf16 v[18:33], v[60:63], v[56:59], v[18:33]
	s_nop 0
	v_addc_co_u32_e32 v93, vcc, 0, v71, vcc
	v_add_co_u32_e32 v94, vcc, s28, v70
	v_mov_b32_e32 v42, v35
	s_nop 0
	v_addc_co_u32_e32 v95, vcc, 0, v71, vcc
	s_waitcnt lgkmcnt(0)
	v_mfma_f32_32x32x16_bf16 v[2:17], v[64:67], v[56:59], v[2:17]
	ds_read_b128 v[48:51], v69 offset:128
	ds_read_b128 v[52:55], v68 offset:17536
	ds_read_b128 v[56:59], v68 offset:17568
	ds_read_b128 v[60:63], v69 offset:160
	v_add_co_u32_e32 v96, vcc, s29, v70
	v_mov_b32_e32 v43, v35
	s_nop 0
	v_addc_co_u32_e32 v97, vcc, 0, v71, vcc
	v_add_co_u32_e32 v98, vcc, s36, v70
	s_waitcnt lgkmcnt(2)
	v_mfma_f32_32x32x16_bf16 v[18:33], v[48:51], v[52:55], v[18:33]
	ds_read_b128 v[48:51], v69 offset:8832
	ds_read_b128 v[64:67], v69 offset:8864
	v_addc_co_u32_e32 v99, vcc, 0, v71, vcc
	v_add_co_u32_e32 v100, vcc, s37, v70
	v_mov_b32_e32 v44, v35
	s_nop 0
	v_addc_co_u32_e32 v101, vcc, 0, v71, vcc
	s_waitcnt lgkmcnt(1)
	v_mfma_f32_32x32x16_bf16 v[2:17], v[48:51], v[52:55], v[2:17]
	v_add_co_u32_e32 v102, vcc, s38, v70
	v_mov_b32_e32 v45, v35
	s_nop 0
	v_addc_co_u32_e32 v103, vcc, 0, v71, vcc
	v_add_co_u32_e32 v104, vcc, s39, v70
	v_mfma_f32_32x32x16_bf16 v[18:33], v[60:63], v[56:59], v[18:33]
	s_nop 0
	v_addc_co_u32_e32 v105, vcc, 0, v71, vcc
	v_add_co_u32_e32 v106, vcc, s40, v70
	v_mov_b32_e32 v46, v35
	s_nop 0
	v_addc_co_u32_e32 v107, vcc, 0, v71, vcc
	v_add_co_u32_e32 v108, vcc, s41, v70
	s_waitcnt lgkmcnt(0)
	v_mfma_f32_32x32x16_bf16 v[2:17], v[64:67], v[56:59], v[2:17]
	v_addc_co_u32_e32 v109, vcc, 0, v71, vcc
	v_add_co_u32_e32 v110, vcc, s42, v70
	ds_read_b128 v[48:51], v69 offset:192
	ds_read_b128 v[52:55], v68 offset:17600
	ds_read_b128 v[56:59], v68 offset:17632
	ds_read_b128 v[60:63], v69 offset:224
	v_addc_co_u32_e32 v111, vcc, 0, v71, vcc
	v_add_co_u32_e32 v112, vcc, s43, v70
	s_waitcnt lgkmcnt(2)
	v_mfma_f32_32x32x16_bf16 v[18:33], v[48:51], v[52:55], v[18:33]
	v_addc_co_u32_e32 v113, vcc, 0, v71, vcc
	ds_read_b128 v[48:51], v69 offset:8896
	ds_read_b128 v[64:67], v69 offset:8928
	v_add_co_u32_e32 v114, vcc, s46, v70
	v_mov_b32_e32 v47, v35
	s_nop 0
	v_addc_co_u32_e32 v115, vcc, 0, v71, vcc
	v_add_co_u32_e32 v116, vcc, s47, v70
	s_waitcnt lgkmcnt(1)
	v_mfma_f32_32x32x16_bf16 v[2:17], v[48:51], v[52:55], v[2:17]
	v_addc_co_u32_e32 v117, vcc, 0, v71, vcc
	v_add_co_u32_e32 v118, vcc, s48, v70
	v_mov_b32_e32 v130, v35
	s_nop 0
	v_addc_co_u32_e32 v119, vcc, 0, v71, vcc
	v_add_co_u32_e32 v120, vcc, s49, v70
	v_mfma_f32_32x32x16_bf16 v[18:33], v[60:63], v[56:59], v[18:33]
	s_nop 0
	v_addc_co_u32_e32 v121, vcc, 0, v71, vcc
	v_add_co_u32_e32 v122, vcc, s52, v70
	v_mov_b32_e32 v131, v35
	s_nop 0
	v_addc_co_u32_e32 v123, vcc, 0, v71, vcc
	v_add_co_u32_e32 v124, vcc, s53, v70
	s_waitcnt lgkmcnt(0)
; DI float clamp448(float x) { return __builtin_amdgcn_fmed3f(x, -448.0f, 448.0f); }
; DI void fft3_unit(unsigned char* lds, const unsigned char* ws, int unit) {
;     ...
;     unsigned char* CAT = const_cast<unsigned char*>(ws) + WS_CAT + (size_t)(b * SEQ + k1) * 1024 + 512 + 32 * w + r;
; #pragma unroll
;     for (int rb = 0; rb < 2; ++rb)
; #pragma unroll
;         for (int i = 0; i < 16; ++i) { const int k2 = 32 * rb + (i & 3) + 8 * (i >> 2) + 4 * h; CAT[(size_t)k2 * 64 * 1024] = (unsigned char)(__builtin_amdgcn_cvt_pk_fp8_f32(clamp448(acc[rb][i] * FOUR_SCALE), 0.f, 0, false) & 0xff); }
;     __syncthreads();
	v_mfma_f32_32x32x16_bf16 v[2:17], v[64:67], v[56:59], v[2:17]
	v_addc_co_u32_e32 v125, vcc, 0, v71, vcc
	v_add_co_u32_e32 v126, vcc, s54, v70
	s_nop 0
	v_add_f32_e32 v18, v18, v18
	v_addc_co_u32_e32 v127, vcc, 0, v71, vcc
	v_add_co_u32_e32 v128, vcc, s55, v70
	v_add_f32_e32 v19, v19, v19
	s_nop 0
	v_addc_co_u32_e32 v129, vcc, 0, v71, vcc
	v_add_co_u32_e32 v48, vcc, s56, v70
	v_med3_f32 v18, v18, s14, v36
	s_nop 0
	v_addc_co_u32_e32 v49, vcc, 0, v71, vcc
	v_add_f32_e32 v20, v20, v20
	v_med3_f32 v19, v19, s14, v36
	v_cvt_pk_fp8_f32 v37, v18, 0
	v_add_co_u32_e32 v50, vcc, s57, v70
	v_add_f32_e32 v21, v21, v21
	v_med3_f32 v20, v20, s14, v36
	v_cvt_pk_fp8_f32 v38, v19, 0
	v_addc_co_u32_e32 v51, vcc, 0, v71, vcc
	v_add_f32_e32 v22, v22, v22
	v_add_f32_e32 v23, v23, v23
	v_add_f32_e32 v24, v24, v24
	v_add_f32_e32 v25, v25, v25
	v_add_f32_e32 v26, v26, v26
	v_add_f32_e32 v27, v27, v27
	v_add_f32_e32 v28, v28, v28
	v_add_f32_e32 v29, v29, v29
	v_add_f32_e32 v30, v30, v30
	v_add_f32_e32 v31, v31, v31
	v_add_f32_e32 v32, v32, v32
	v_add_f32_e32 v33, v33, v33
	v_add_f32_e32 v2, v2, v2
	v_add_f32_e32 v3, v3, v3
	v_add_f32_e32 v4, v4, v4
	v_add_f32_e32 v5, v5, v5
	v_add_f32_e32 v6, v6, v6
	v_add_f32_e32 v7, v7, v7
	v_add_f32_e32 v8, v8, v8
	v_add_f32_e32 v9, v9, v9
	v_add_f32_e32 v10, v10, v10
	v_add_f32_e32 v11, v11, v11
	v_add_f32_e32 v12, v12, v12
	v_add_f32_e32 v13, v13, v13
	v_add_f32_e32 v14, v14, v14
	v_add_f32_e32 v15, v15, v15
	v_add_f32_e32 v16, v16, v16
	v_add_f32_e32 v17, v17, v17
	v_med3_f32 v21, v21, s14, v36
	v_cvt_pk_fp8_f32 v39, v20, 0
	v_mov_b32_e32 v132, v35
	v_mov_b32_e32 v133, v35
	v_mov_b32_e32 v134, v35
	v_mov_b32_e32 v135, v35
	v_mov_b32_e32 v136, v35
	v_mov_b32_e32 v137, v35
	v_mov_b32_e32 v138, v35
	v_mov_b32_e32 v139, v35
	v_mov_b32_e32 v140, v35
	v_mov_b32_e32 v141, v35
	v_mov_b32_e32 v142, v35
	v_mov_b32_e32 v143, v35
	v_mov_b32_e32 v144, v35
	v_mov_b32_e32 v145, v35
	v_mov_b32_e32 v146, v35
	v_mov_b32_e32 v147, v35
	v_mov_b32_e32 v148, v35
	v_mov_b32_e32 v149, v35
	v_mov_b32_e32 v150, v35
	s_cmpk_lt_i32 s4, 0x200
	v_add_co_u32_e32 v52, vcc, 0x2b184000, v70
	v_med3_f32 v22, v22, s14, v36
	v_med3_f32 v23, v23, s14, v36
	v_med3_f32 v24, v24, s14, v36
	v_med3_f32 v25, v25, s14, v36
	v_med3_f32 v26, v26, s14, v36
	v_med3_f32 v27, v27, s14, v36
	v_med3_f32 v28, v28, s14, v36
	v_med3_f32 v29, v29, s14, v36
	v_med3_f32 v30, v30, s14, v36
	v_med3_f32 v31, v31, s14, v36
	v_med3_f32 v32, v32, s14, v36
	v_med3_f32 v33, v33, s14, v36
	v_med3_f32 v2, v2, s14, v36
	v_med3_f32 v3, v3, s14, v36
	v_med3_f32 v4, v4, s14, v36
	v_med3_f32 v5, v5, s14, v36
	v_med3_f32 v6, v6, s14, v36
	v_med3_f32 v7, v7, s14, v36
	v_med3_f32 v8, v8, s14, v36
	v_med3_f32 v9, v9, s14, v36
	v_med3_f32 v10, v10, s14, v36
	v_med3_f32 v11, v11, s14, v36
	v_med3_f32 v12, v12, s14, v36
	v_med3_f32 v13, v13, s14, v36
	v_med3_f32 v14, v14, s14, v36
	v_med3_f32 v15, v15, s14, v36
	v_med3_f32 v16, v16, s14, v36
	v_med3_f32 v17, v17, s14, v36
	v_cvt_pk_fp8_f32 v40, v21, 0
	v_addc_co_u32_e32 v53, vcc, 0, v71, vcc
	v_cvt_pk_fp8_f32 v41, v22, 0
	v_cvt_pk_fp8_f32 v42, v23, 0
	v_cvt_pk_fp8_f32 v43, v24, 0
	v_cvt_pk_fp8_f32 v44, v25, 0
	v_cvt_pk_fp8_f32 v45, v26, 0
	v_cvt_pk_fp8_f32 v46, v27, 0
	v_cvt_pk_fp8_f32 v47, v28, 0
	v_cvt_pk_fp8_f32 v130, v29, 0
	v_cvt_pk_fp8_f32 v131, v30, 0
	v_cvt_pk_fp8_f32 v132, v31, 0
	v_cvt_pk_fp8_f32 v133, v32, 0
	v_cvt_pk_fp8_f32 v134, v33, 0
	v_cvt_pk_fp8_f32 v135, v2, 0
	v_cvt_pk_fp8_f32 v136, v3, 0
	v_cvt_pk_fp8_f32 v137, v4, 0
	v_cvt_pk_fp8_f32 v138, v5, 0
	v_cvt_pk_fp8_f32 v139, v6, 0
	v_cvt_pk_fp8_f32 v140, v7, 0
	v_cvt_pk_fp8_f32 v141, v8, 0
	v_cvt_pk_fp8_f32 v142, v9, 0
	v_cvt_pk_fp8_f32 v143, v10, 0
	v_cvt_pk_fp8_f32 v144, v11, 0
	v_cvt_pk_fp8_f32 v145, v12, 0
	v_cvt_pk_fp8_f32 v146, v13, 0
	v_cvt_pk_fp8_f32 v147, v14, 0
	v_cvt_pk_fp8_f32 v148, v15, 0
	v_cvt_pk_fp8_f32 v149, v16, 0
	v_cvt_pk_fp8_f32 v150, v17, 0
	global_store_byte v[72:73], v37, off offset:512
	global_store_byte v[74:75], v38, off offset:512
	global_store_byte v[76:77], v39, off offset:512
	global_store_byte v[78:79], v40, off offset:512
	global_store_byte v[80:81], v41, off offset:512
	global_store_byte v[82:83], v42, off offset:512
	global_store_byte v[84:85], v43, off offset:512
	global_store_byte v[86:87], v44, off offset:512
	global_store_byte v[88:89], v45, off offset:512
	global_store_byte v[90:91], v46, off offset:512
	global_store_byte v[92:93], v47, off offset:512
	global_store_byte v[94:95], v130, off offset:512
	global_store_byte v[96:97], v131, off offset:512
	global_store_byte v[98:99], v132, off offset:512
	global_store_byte v[100:101], v133, off offset:512
	global_store_byte v[102:103], v134, off offset:512
	global_store_byte v[104:105], v135, off offset:512
	global_store_byte v[106:107], v136, off offset:512
	global_store_byte v[108:109], v137, off offset:512
	global_store_byte v[110:111], v138, off offset:512
	global_store_byte v[112:113], v139, off offset:512
	global_store_byte v[114:115], v140, off offset:512
	global_store_byte v[116:117], v141, off offset:512
	global_store_byte v[118:119], v142, off offset:512
	global_store_byte v[120:121], v143, off offset:512
	global_store_byte v[122:123], v144, off offset:512
	global_store_byte v[124:125], v145, off offset:512
	global_store_byte v[126:127], v146, off offset:512
	global_store_byte v[128:129], v147, off offset:512
	global_store_byte v[48:49], v148, off offset:512
	global_store_byte v[50:51], v149, off offset:512
	global_store_byte v[52:53], v150, off offset:512
	s_barrier
	s_cbranch_scc1 .LBB0_685
